# speedup vs baseline: 1.0160x; 1.0037x over previous
.LBB3_2:
	s_or_b64 exec, exec, s[10:11]
	s_waitcnt vmcnt(21)
	v_cvt_f32_f16_e32 v36, v4
	v_cvt_f32_f16_sdwa v37, v4 dst_sel:DWORD dst_unused:UNUSED_PAD src0_sel:WORD_1
	v_cvt_f32_f16_e32 v4, v5
	v_cvt_f32_f16_sdwa v5, v5 dst_sel:DWORD dst_unused:UNUSED_PAD src0_sel:WORD_1
	s_waitcnt vmcnt(20)
	v_cvt_f32_f16_e32 v38, v8
	v_cvt_f32_f16_sdwa v39, v8 dst_sel:DWORD dst_unused:UNUSED_PAD src0_sel:WORD_1
	s_waitcnt vmcnt(19)
	v_cvt_f32_f16_e32 v40, v12
	v_cvt_f32_f16_sdwa v41, v12 dst_sel:DWORD dst_unused:UNUSED_PAD src0_sel:WORD_1
	v_cvt_f32_f16_e32 v8, v9
	v_cvt_f32_f16_sdwa v9, v9 dst_sel:DWORD dst_unused:UNUSED_PAD src0_sel:WORD_1
	s_waitcnt vmcnt(18)
	v_cvt_f32_f16_e32 v42, v16
	v_cvt_f32_f16_sdwa v43, v16 dst_sel:DWORD dst_unused:UNUSED_PAD src0_sel:WORD_1
	v_cvt_f32_f16_e32 v12, v13
	v_cvt_f32_f16_sdwa v13, v13 dst_sel:DWORD dst_unused:UNUSED_PAD src0_sel:WORD_1
	v_cvt_f32_f16_e32 v16, v17
	s_waitcnt vmcnt(17)
	v_cvt_f32_f16_e32 v44, v20
	v_cvt_f32_f16_sdwa v45, v20 dst_sel:DWORD dst_unused:UNUSED_PAD src0_sel:WORD_1
	v_cvt_f32_f16_sdwa v17, v17 dst_sel:DWORD dst_unused:UNUSED_PAD src0_sel:WORD_1
	v_pk_add_f32 v[36:37], v[36:37], 0 op_sel_hi:[1,0]
	v_pk_add_f32 v[4:5], v[4:5], 0 op_sel_hi:[1,0]
	v_pk_add_f32 v[36:37], v[36:37], v[38:39]
	v_pk_add_f32 v[4:5], v[4:5], v[8:9]
	v_pk_add_f32 v[8:9], v[36:37], v[40:41]
	v_cvt_f32_f16_e32 v20, v21
	v_cvt_f32_f16_sdwa v21, v21 dst_sel:DWORD dst_unused:UNUSED_PAD src0_sel:WORD_1
	v_pk_add_f32 v[4:5], v[4:5], v[12:13]
	v_pk_add_f32 v[8:9], v[8:9], v[42:43]
	s_waitcnt vmcnt(16)
	v_cvt_f32_f16_e32 v46, v24
	v_cvt_f32_f16_sdwa v47, v24 dst_sel:DWORD dst_unused:UNUSED_PAD src0_sel:WORD_1
	v_pk_add_f32 v[12:13], v[4:5], v[16:17]
	v_pk_add_f32 v[4:5], v[8:9], v[44:45]
	v_cvt_f32_f16_e32 v8, v25
	v_cvt_f32_f16_sdwa v9, v25 dst_sel:DWORD dst_unused:UNUSED_PAD src0_sel:WORD_1
	s_waitcnt vmcnt(15)
	v_cvt_f32_f16_e32 v48, v28
	v_cvt_f32_f16_sdwa v49, v28 dst_sel:DWORD dst_unused:UNUSED_PAD src0_sel:WORD_1
	v_cvt_f32_f16_e32 v16, v29
	v_cvt_f32_f16_sdwa v17, v29 dst_sel:DWORD dst_unused:UNUSED_PAD src0_sel:WORD_1
	s_waitcnt vmcnt(14)
	v_cvt_f32_f16_e32 v50, v32
	v_cvt_f32_f16_sdwa v51, v32 dst_sel:DWORD dst_unused:UNUSED_PAD src0_sel:WORD_1
	v_cvt_f32_f16_e32 v24, v33
	v_cvt_f32_f16_sdwa v25, v33 dst_sel:DWORD dst_unused:UNUSED_PAD src0_sel:WORD_1
	v_pk_add_f32 v[12:13], v[12:13], v[20:21]
	v_pk_add_f32 v[4:5], v[4:5], v[46:47]
	v_pk_add_f32 v[8:9], v[12:13], v[8:9]
	v_pk_add_f32 v[4:5], v[4:5], v[48:49]
	v_pk_add_f32 v[8:9], v[8:9], v[16:17]
	v_pk_add_f32 v[4:5], v[4:5], v[50:51]
	v_pk_add_f32 v[8:9], v[8:9], v[24:25]
	v_cvt_pk_bf16_f32 v4, v4, v5
	v_cvt_pk_bf16_f32 v5, v8, v9
	v_cvt_f32_f16_e32 v8, v6
	v_cvt_f32_f16_sdwa v9, v6 dst_sel:DWORD dst_unused:UNUSED_PAD src0_sel:WORD_1
	v_cvt_f32_f16_e32 v12, v10
	v_cvt_f32_f16_sdwa v13, v10 dst_sel:DWORD dst_unused:UNUSED_PAD src0_sel:WORD_1
	v_cvt_f32_f16_e32 v16, v14
	v_cvt_f32_f16_sdwa v17, v14 dst_sel:DWORD dst_unused:UNUSED_PAD src0_sel:WORD_1
	v_cvt_f32_f16_e32 v20, v18
	v_cvt_f32_f16_sdwa v21, v18 dst_sel:DWORD dst_unused:UNUSED_PAD src0_sel:WORD_1
	v_pk_add_f32 v[8:9], v[8:9], 0 op_sel_hi:[1,0]
	v_cvt_f32_f16_e32 v24, v34
	v_pk_add_f32 v[8:9], v[8:9], v[12:13]
	v_cvt_f32_f16_e32 v12, v22
	v_cvt_f32_f16_sdwa v13, v22 dst_sel:DWORD dst_unused:UNUSED_PAD src0_sel:WORD_1
	v_pk_add_f32 v[8:9], v[8:9], v[16:17]
	v_cvt_f32_f16_e32 v16, v26
	v_cvt_f32_f16_sdwa v17, v26 dst_sel:DWORD dst_unused:UNUSED_PAD src0_sel:WORD_1
	v_pk_add_f32 v[8:9], v[8:9], v[20:21]
	v_cvt_f32_f16_e32 v20, v30
	v_cvt_f32_f16_sdwa v21, v30 dst_sel:DWORD dst_unused:UNUSED_PAD src0_sel:WORD_1
	v_cvt_f32_f16_sdwa v25, v34 dst_sel:DWORD dst_unused:UNUSED_PAD src0_sel:WORD_1
	v_pk_add_f32 v[8:9], v[8:9], v[12:13]
	v_cvt_f32_f16_e32 v10, v11
	v_pk_add_f32 v[8:9], v[8:9], v[16:17]
	v_cvt_f32_f16_sdwa v11, v11 dst_sel:DWORD dst_unused:UNUSED_PAD src0_sel:WORD_1
	v_pk_add_f32 v[8:9], v[8:9], v[20:21]
	v_cvt_f32_f16_e32 v12, v15
	v_pk_add_f32 v[8:9], v[8:9], v[24:25]
	v_cvt_f32_f16_sdwa v13, v15 dst_sel:DWORD dst_unused:UNUSED_PAD src0_sel:WORD_1
	v_cvt_pk_bf16_f32 v6, v8, v9
	v_cvt_f32_f16_e32 v8, v7
	v_cvt_f32_f16_sdwa v9, v7 dst_sel:DWORD dst_unused:UNUSED_PAD src0_sel:WORD_1
	v_cvt_f32_f16_e32 v14, v19
	v_cvt_f32_f16_sdwa v15, v19 dst_sel:DWORD dst_unused:UNUSED_PAD src0_sel:WORD_1
	v_cvt_f32_f16_e32 v16, v35
	v_pk_add_f32 v[8:9], v[8:9], 0 op_sel_hi:[1,0]
	v_cvt_f32_f16_sdwa v17, v35 dst_sel:DWORD dst_unused:UNUSED_PAD src0_sel:WORD_1
	v_pk_add_f32 v[8:9], v[8:9], v[10:11]
	v_cvt_f32_f16_e32 v10, v23
	v_cvt_f32_f16_sdwa v11, v23 dst_sel:DWORD dst_unused:UNUSED_PAD src0_sel:WORD_1
	v_pk_add_f32 v[8:9], v[8:9], v[12:13]
	v_cvt_f32_f16_e32 v12, v27
	v_cvt_f32_f16_sdwa v13, v27 dst_sel:DWORD dst_unused:UNUSED_PAD src0_sel:WORD_1
	v_pk_add_f32 v[8:9], v[8:9], v[14:15]
	v_cvt_f32_f16_e32 v14, v31
	v_cvt_f32_f16_sdwa v15, v31 dst_sel:DWORD dst_unused:UNUSED_PAD src0_sel:WORD_1
	v_pk_add_f32 v[8:9], v[8:9], v[10:11]
	s_nop 0
	v_pk_add_f32 v[8:9], v[8:9], v[12:13]
	v_lshlrev_b32_e32 v12, 6, v58
	v_pk_add_f32 v[8:9], v[8:9], v[14:15]
	v_ashrrev_i32_e32 v13, 31, v12
	v_pk_add_f32 v[8:9], v[8:9], v[16:17]
	v_cvt_pk_bf16_f32 v7, v8, v9
	v_and_b32_e32 v8, 0x1e0000, v59
	v_mov_b32_e32 v9, 0
	v_lshl_add_u64 v[10:11], s[54:55], 0, v[8:9]
	v_lshl_add_u64 v[10:11], v[12:13], 1, v[10:11]
	v_lshlrev_b32_e32 v8, 1, v54
	v_lshl_add_u64 v[8:9], v[10:11], 0, v[8:9]
	global_store_dwordx4 v[8:9], v[4:7], off
	s_load_dwordx2 s[10:11], s[0:1], 0x10
	s_load_dwordx2 s[56:57], s[0:1], 0x10
	v_lshrrev_b32_e32 v206, 8, v0
	v_lshrrev_b32_e32 v34, 2, v0
	v_cmp_eq_u32_e64 s[2:3], 1, v206
	s_and_saveexec_b64 s[14:15], s[2:3]
	s_cbranch_execz .LBB3_4
	s_barrier
.LBB3_4:
	s_or_b64 exec, exec, s[14:15]
	v_bfe_u32 v38, v0, 4, 2
	v_and_b32_e32 v40, 16, v0
	v_and_b32_e32 v35, 15, v0
	v_bfe_u32 v36, v0, 6, 2
	v_and_or_b32 v198, v34, 8, v40
	v_bitop3_b32 v34, v38, v0, 7 bitop3:0x78
	v_lshl_or_b32 v209, v36, 5, v35
	v_lshlrev_b32_e32 v228, 7, v209
	v_and_b32_e32 v229, 1, v0
	v_and_b32_e32 v228, 0x3f00, v228
	v_lshl_or_b32 v228, v229, 6, v228
	v_lshl_or_b32 v228, v198, 1, v228
	v_lshlrev_b32_e32 v211, 4, v34
	v_lshlrev_b32_e32 v34, 12, v36
	v_lshlrev_b32_e32 v35, 7, v35
	s_add_i32 s2, 0, 0x10000
	v_add3_u32 v212, s2, v34, v35
	s_add_i32 s2, 0, 0x10800
	v_add3_u32 v214, s2, v34, v35
	s_add_i32 s2, 0, 0x14000
	s_load_dwordx2 s[14:15], s[0:1], 0x20
	v_and_b32_e32 v2, 0x100, v0
	v_and_b32_e32 v3, 48, v0
	s_add_i32 s0, 0, 0x20000
	v_add3_u32 v215, s2, v34, v35
	s_add_i32 s2, 0, 0x14800
	v_add3_u32 v207, s0, v3, v2
	v_add3_u32 v216, s2, v34, v35
	s_add_i32 s2, 0, 0x18000
	s_waitcnt vmcnt(6)
	s_barrier
	s_barrier
	ds_read_b128 v[18:21], v207
	ds_read_b128 v[2:5], v207 offset:64
	ds_read_b128 v[26:29], v207 offset:128
	ds_read_b128 v[10:13], v207 offset:192
	ds_read_b128 v[22:25], v207 offset:512
	ds_read_b128 v[6:9], v207 offset:576
	ds_read_b128 v[30:33], v207 offset:640
	ds_read_b128 v[14:17], v207 offset:704
	v_add3_u32 v218, s2, v34, v35
	s_add_i32 s2, 0, 0x18800
	v_add3_u32 v219, s2, v34, v35
	s_add_i32 s2, 0, 0x1c000
	v_and_b32_e32 v37, 63, v0
	v_and_b32_e32 v39, 7, v0
	v_add3_u32 v220, s2, v34, v35
	s_add_i32 s2, 0, 0x1c800
	v_lshlrev_b32_e32 v194, 4, v37
	v_mov_b32_e32 v195, 0
	v_bitop3_b32 v36, v38, v39, 4 bitop3:0x36
	v_add3_u32 v221, s2, v34, v35
	v_lshlrev_b32_e32 v34, 6, v0
	v_add_u32_e32 v208, s0, v194
	v_lshl_add_u64 v[196:197], s[16:17], 0, v[194:195]
	v_lshlrev_b32_e32 v213, 4, v36
	v_lshlrev_b32_e32 v36, 13, v206
	v_and_b32_e32 v194, 64, v34
	v_mbcnt_lo_u32_b32 v34, -1, 0
	v_cmp_gt_u32_e64 s[0:1], 16, v37
	v_add3_u32 v217, 0, v36, v35
	v_mbcnt_hi_u32_b32 v222, -1, v34
	s_waitcnt lgkmcnt(0)
	v_mov_b64_e32 v[48:49], v[16:17]
	v_mov_b64_e32 v[120:121], v[32:33]
	v_mov_b64_e32 v[36:37], v[8:9]
	v_mov_b64_e32 v[84:85], v[24:25]
	v_mov_b64_e32 v[52:53], v[16:17]
	v_mov_b64_e32 v[60:61], v[16:17]
	v_mov_b64_e32 v[124:125], v[32:33]
	v_mov_b64_e32 v[128:129], v[32:33]
	v_mov_b64_e32 v[40:41], v[8:9]
	v_mov_b64_e32 v[44:45], v[8:9]
	v_mov_b64_e32 v[88:89], v[24:25]
	v_mov_b64_e32 v[92:93], v[24:25]
	v_mov_b64_e32 v[56:57], v[12:13]
	v_mov_b64_e32 v[96:97], v[28:29]
	v_mov_b64_e32 v[64:65], v[4:5]
	v_mov_b64_e32 v[100:101], v[20:21]
	v_mov_b64_e32 v[68:69], v[12:13]
	v_mov_b64_e32 v[72:73], v[12:13]
	v_mov_b64_e32 v[104:105], v[28:29]
	v_mov_b64_e32 v[108:109], v[28:29]
	v_mov_b64_e32 v[76:77], v[4:5]
	v_mov_b64_e32 v[80:81], v[4:5]
	v_mov_b64_e32 v[112:113], v[20:21]
	v_mov_b64_e32 v[116:117], v[20:21]
	s_mov_b32 s13, 0
	s_add_i32 s36, s20, 0xc000
	v_lshlrev_b32_e32 v210, 6, v206
	s_add_i32 s37, s20, 0xe000
	v_lshl_add_u64 v[200:201], s[10:11], 0, v[194:195]
	s_mov_b32 s10, s6
	s_mov_b32 s11, s7
	s_mov_b32 s38, 0x7fffff00
	s_mov_b32 s39, 0x7ffff700
	v_mov_b32_e32 v223, 0x800
	v_mov_b32_e32 v224, 0x4000
	s_mov_b32 s40, 0
	v_mov_b32_e32 v225, 0x4800
	v_mov_b64_e32 v[46:47], v[14:15]
	v_mov_b64_e32 v[118:119], v[30:31]
	v_mov_b64_e32 v[34:35], v[6:7]
	v_mov_b64_e32 v[82:83], v[22:23]
	v_mov_b64_e32 v[50:51], v[14:15]
	v_mov_b64_e32 v[58:59], v[14:15]
	v_mov_b64_e32 v[122:123], v[30:31]
	v_mov_b64_e32 v[126:127], v[30:31]
	v_mov_b64_e32 v[38:39], v[6:7]
	v_mov_b64_e32 v[42:43], v[6:7]
	v_mov_b64_e32 v[86:87], v[22:23]
	v_mov_b64_e32 v[90:91], v[22:23]
	v_mov_b64_e32 v[54:55], v[10:11]
	v_mov_b64_e32 v[94:95], v[26:27]
	v_mov_b64_e32 v[62:63], v[2:3]
	v_mov_b64_e32 v[98:99], v[18:19]
	v_mov_b64_e32 v[66:67], v[10:11]
	v_mov_b64_e32 v[70:71], v[10:11]
	v_mov_b64_e32 v[102:103], v[26:27]
	v_mov_b64_e32 v[106:107], v[26:27]
	v_mov_b64_e32 v[74:75], v[2:3]
	v_mov_b64_e32 v[78:79], v[2:3]
	v_mov_b64_e32 v[110:111], v[18:19]
	v_mov_b64_e32 v[114:115], v[18:19]
	s_branch .LBB3_6

.LBB3_11:
	s_lshl_b32 s58, s42, 7
	s_add_i32 s59, s41, 0x400
	s_lshr_b32 s59, s59, 6
	s_bfe_u32 s60, s20, 0x1000c
	s_add_i32 s59, s59, s60
	s_lshl_b32 s59, s59, 19
	s_add_u32 s58, s58, s59
	s_add_u32 s58, s56, s58
	s_addc_u32 s59, s57, 0
	s_add_u32 s60, s58, 0x4000
	s_addc_u32 s61, s59, 0
	s_add_u32 s62, s58, 0x100000
	s_addc_u32 s63, s59, 0
	s_add_u32 s64, s62, 0x4000
	s_addc_u32 s65, s63, 0
	v_and_b32_e32 v133, 64, v222
	v_xor_b32_e32 v132, 16, v222
	v_add_u32_e32 v133, 64, v133
	v_cmp_lt_i32_e64 s[2:3], v132, v133
	v_exp_f32_e32 v134, v114
	v_exp_f32_e32 v136, v116
	v_cndmask_b32_e64 v132, v222, v132, s[2:3]
	v_lshlrev_b32_e32 v140, 2, v132
	v_xor_b32_e32 v132, 32, v222
	v_exp_f32_e32 v137, v117
	v_exp_f32_e32 v135, v115
	v_cmp_lt_i32_e64 s[2:3], v132, v133
	v_or_b32_e32 v130, s42, v209
	s_nop 0
	v_cndmask_b32_e64 v132, v222, v132, s[2:3]
	s_lshr_b32 s2, s41, 7
	v_add_u32_e32 v194, s2, v206
	v_lshlrev_b32_e32 v139, 2, v132
	v_lshlrev_b64 v[132:133], 14, v[194:195]
	v_pk_add_f32 v[136:137], v[136:137], 1.0 op_sel_hi:[1,0]
	v_pk_add_f32 v[144:145], v[134:135], 1.0 op_sel_hi:[1,0]
	v_rcp_f32_e64 v143, -v137
	v_rcp_f32_e64 v142, -v136
	v_rcp_f32_e64 v149, -v145
	v_rcp_f32_e64 v148, -v144
	v_exp_f32_e32 v154, v80
	v_pk_fma_f32 v[152:153], v[142:143], 2.0, 1.0 op_sel_hi:[1,0,0]
	v_exp_f32_e32 v155, v81
	v_pk_fma_f32 v[142:143], v[148:149], 2.0, 1.0 op_sel_hi:[1,0,0]
	v_exp_f32_e32 v148, v78
	v_exp_f32_e32 v149, v79
	v_pk_add_f32 v[154:155], v[154:155], 1.0 op_sel_hi:[1,0]
	v_cvt_pk_bf16_f32 v142, v142, v143
	v_rcp_f32_e64 v157, -v155
	v_pk_add_f32 v[148:149], v[148:149], 1.0 op_sel_hi:[1,0]
	v_rcp_f32_e64 v156, -v154
	v_rcp_f32_e64 v159, -v149
	v_rcp_f32_e64 v158, -v148
	v_cvt_pk_bf16_f32 v143, v152, v153
	v_pk_fma_f32 v[152:153], v[156:157], 2.0, 1.0 op_sel_hi:[1,0,0]
	v_pk_mul_f32 v[148:149], v[144:145], v[148:149]
	v_pk_fma_f32 v[156:157], v[158:159], 2.0, 1.0 op_sel_hi:[1,0,0]
	v_cvt_pk_bf16_f32 v145, v152, v153
	v_cvt_pk_bf16_f32 v144, v156, v157
	v_exp_f32_e32 v152, v106
	v_exp_f32_e32 v153, v107
	v_exp_f32_e32 v156, v108
	v_exp_f32_e32 v157, v109
	v_pk_mul_f32 v[136:137], v[136:137], v[154:155]
	v_pk_add_f32 v[152:153], v[152:153], 1.0 op_sel_hi:[1,0]
	v_pk_add_f32 v[116:117], v[116:117], 0 op_sel_hi:[1,0]
	v_pk_add_f32 v[156:157], v[156:157], 1.0 op_sel_hi:[1,0]
	v_rcp_f32_e64 v163, -v153
	v_rcp_f32_e64 v161, -v157
	v_rcp_f32_e64 v160, -v156
	v_rcp_f32_e64 v162, -v152
	v_pk_mul_f32 v[148:149], v[148:149], v[152:153]
	v_pk_mul_f32 v[136:137], v[136:137], v[156:157]
	v_exp_f32_e32 v152, v70
	v_exp_f32_e32 v156, v72
	v_exp_f32_e32 v157, v73
	v_exp_f32_e32 v153, v71
	v_pk_add_f32 v[114:115], v[114:115], 0 op_sel_hi:[1,0]
	v_pk_add_f32 v[154:155], v[116:117], v[80:81]
	v_pk_add_f32 v[158:159], v[114:115], v[78:79]
	v_pk_add_f32 v[108:109], v[154:155], v[108:109]
	v_pk_add_f32 v[154:155], v[156:157], 1.0 op_sel_hi:[1,0]
	v_pk_add_f32 v[152:153], v[152:153], 1.0 op_sel_hi:[1,0]
	v_pk_add_f32 v[106:107], v[158:159], v[106:107]
	v_rcp_f32_e64 v157, -v155
	v_rcp_f32_e64 v156, -v154
	v_rcp_f32_e64 v159, -v153
	v_rcp_f32_e64 v158, -v152
	v_add_u32_e32 v138, s43, v207
	v_permlane16_swap_b32_e32 v142, v144
	v_permlane16_swap_b32_e32 v143, v145
	ds_read_b128 v[114:117], v138
	ds_read_b128 v[78:81], v138 offset:64
	global_store_dwordx4 v228, v[142:145], s[58:59] nt
	s_bitcmp1_b32 s20, 12
	s_cbranch_scc1 .Lg1_noX
	s_barrier
.Lg1_noX:
	v_pk_fma_f32 v[156:157], v[156:157], 2.0, 1.0 op_sel_hi:[1,0,0]
	v_pk_mul_f32 v[154:155], v[136:137], v[154:155]
	v_pk_fma_f32 v[144:145], v[160:161], 2.0, 1.0 op_sel_hi:[1,0,0]
	v_pk_fma_f32 v[142:143], v[162:163], 2.0, 1.0 op_sel_hi:[1,0,0]
	v_pk_mul_f32 v[148:149], v[148:149], v[152:153]
	v_cvt_pk_bf16_f32 v142, v142, v143
	v_cvt_pk_bf16_f32 v143, v144, v145
	v_pk_fma_f32 v[144:145], v[158:159], 2.0, 1.0 op_sel_hi:[1,0,0]
	v_pk_add_f32 v[152:153], v[108:109], v[72:73]
	v_cvt_pk_bf16_f32 v144, v144, v145
	v_cvt_pk_bf16_f32 v145, v156, v157
	s_nop 0
	v_permlane16_swap_b32_e32 v142, v144
	v_permlane16_swap_b32_e32 v143, v145
	v_pk_add_f32 v[158:159], v[106:107], v[70:71]
	ds_read_b128 v[106:109], v138 offset:128
	ds_read_b128 v[70:73], v138 offset:192
	global_store_dwordx4 v228, v[142:145], s[58:59] offset:128 nt
	v_exp_f32_e32 v136, v90
	v_exp_f32_e32 v137, v91
	v_exp_f32_e32 v142, v92
	v_exp_f32_e32 v143, v93
	v_pk_add_f32 v[150:151], v[136:137], 1.0 op_sel_hi:[1,0]
	v_pk_add_f32 v[142:143], v[142:143], 1.0 op_sel_hi:[1,0]
	v_rcp_f32_e64 v161, -v151
	v_rcp_f32_e64 v157, -v143
	v_rcp_f32_e64 v156, -v142
	v_rcp_f32_e64 v160, -v150
	v_pk_mul_f32 v[148:149], v[148:149], v[150:151]
	v_pk_mul_f32 v[150:151], v[154:155], v[142:143]
	v_exp_f32_e32 v142, v42
	v_exp_f32_e32 v154, v44
	v_exp_f32_e32 v155, v45
	v_exp_f32_e32 v143, v43
	v_pk_add_f32 v[92:93], v[152:153], v[92:93]
	v_pk_add_f32 v[152:153], v[154:155], 1.0 op_sel_hi:[1,0]
	v_pk_add_f32 v[154:155], v[142:143], 1.0 op_sel_hi:[1,0]
	v_pk_fma_f32 v[144:145], v[156:157], 2.0, 1.0 op_sel_hi:[1,0,0]
	v_pk_fma_f32 v[156:157], v[160:161], 2.0, 1.0 op_sel_hi:[1,0,0]
	v_pk_add_f32 v[90:91], v[158:159], v[90:91]
	v_rcp_f32_e64 v159, -v153
	v_rcp_f32_e64 v158, -v152
	v_rcp_f32_e64 v161, -v155
	v_rcp_f32_e64 v160, -v154
	v_cvt_pk_bf16_f32 v142, v156, v157
	v_cvt_pk_bf16_f32 v143, v144, v145
	v_pk_fma_f32 v[156:157], v[158:159], 2.0, 1.0 op_sel_hi:[1,0,0]
	v_pk_fma_f32 v[144:145], v[160:161], 2.0, 1.0 op_sel_hi:[1,0,0]
	v_exp_f32_e32 v158, v128
	v_cvt_pk_bf16_f32 v144, v144, v145
	v_cvt_pk_bf16_f32 v145, v156, v157
	v_exp_f32_e32 v156, v126
	v_exp_f32_e32 v159, v129
	v_exp_f32_e32 v157, v127
	v_pk_mul_f32 v[150:151], v[150:151], v[152:153]
	v_pk_mul_f32 v[148:149], v[148:149], v[154:155]
	v_pk_add_f32 v[158:159], v[158:159], 1.0 op_sel_hi:[1,0]
	v_pk_add_f32 v[156:157], v[156:157], 1.0 op_sel_hi:[1,0]
	v_rcp_f32_e64 v163, -v157
	v_rcp_f32_e64 v162, -v156
	v_pk_mul_f32 v[146:147], v[148:149], v[156:157]
	v_pk_mul_f32 v[148:149], v[150:151], v[158:159]
	v_exp_f32_e32 v150, v58
	v_exp_f32_e32 v156, v60
	v_exp_f32_e32 v157, v61
	v_exp_f32_e32 v151, v59
	v_pk_add_f32 v[152:153], v[92:93], v[44:45]
	v_pk_add_f32 v[154:155], v[90:91], v[42:43]
	v_pk_add_f32 v[128:129], v[152:153], v[128:129]
	v_pk_add_f32 v[152:153], v[156:157], 1.0 op_sel_hi:[1,0]
	v_pk_add_f32 v[150:151], v[150:151], 1.0 op_sel_hi:[1,0]
	v_pk_mul_f32 v[148:149], v[148:149], v[152:153]
	v_pk_mul_f32 v[146:147], v[146:147], v[150:151]
	v_pk_add_f32 v[126:127], v[154:155], v[126:127]
	v_log_f32_e32 v131, v146
	v_log_f32_e32 v146, v147
	v_log_f32_e32 v147, v148
	v_log_f32_e32 v148, v149
	v_pk_add_f32 v[60:61], v[128:129], v[60:61]
	v_pk_add_f32 v[58:59], v[126:127], v[58:59]
	v_add_f32_e32 v126, v131, v146
	v_add_f32_e32 v127, v147, v148
	v_add_f32_e32 v58, v58, v59
	v_add_f32_e32 v59, v60, v61
	v_add_f32_e32 v126, v126, v127
	v_add_f32_e32 v58, v58, v59
	v_add_f32_e32 v126, 0xc2000000, v126
	v_mul_f32_e32 v131, 0xbeb17218, v58
	v_fmac_f32_e32 v131, 0x3f317218, v126
	v_rcp_f32_e64 v161, -v159
	v_rcp_f32_e64 v160, -v158
	ds_bpermute_b32 v148, v140, v131
	v_rcp_f32_e64 v155, -v153
	v_rcp_f32_e64 v154, -v152
	v_permlane16_swap_b32_e32 v142, v144
	v_permlane16_swap_b32_e32 v143, v145
	ds_read_b128 v[90:93], v138 offset:512
	ds_read_b128 v[42:45], v138 offset:576
	global_store_dwordx4 v228, v[142:145], s[62:63] nt
	v_rcp_f32_e64 v157, -v151
	v_rcp_f32_e64 v156, -v150
	v_pk_fma_f32 v[142:143], v[160:161], 2.0, 1.0 op_sel_hi:[1,0,0]
	v_pk_fma_f32 v[144:145], v[162:163], 2.0, 1.0 op_sel_hi:[1,0,0]
	s_waitcnt lgkmcnt(0)
	v_add_f32_e32 v131, v131, v148
	v_cvt_pk_bf16_f32 v144, v144, v145
	v_cvt_pk_bf16_f32 v145, v142, v143
	v_pk_fma_f32 v[142:143], v[154:155], 2.0, 1.0 op_sel_hi:[1,0,0]
	ds_read_b128 v[126:129], v138 offset:640
	ds_read_b128 v[58:61], v138 offset:704
	v_cvt_pk_bf16_f32 v147, v142, v143
	ds_bpermute_b32 v142, v139, v131
	v_pk_fma_f32 v[154:155], v[156:157], 2.0, 1.0 op_sel_hi:[1,0,0]
	v_lshl_add_u64 v[132:133], s[14:15], 0, v[132:133]
	v_cvt_pk_bf16_f32 v146, v154, v155
	s_nop 1
	v_permlane16_swap_b32_e32 v144, v146
	v_permlane16_swap_b32_e32 v145, v147
	global_store_dwordx4 v228, v[144:147], s[62:63] offset:128 nt
	s_and_saveexec_b64 s[2:3], s[0:1]
	s_cbranch_execz .LBB3_13
	s_waitcnt lgkmcnt(0)
	v_add_f32_e32 v144, v131, v142
	v_mov_b32_e32 v131, v195
	v_lshl_add_u64 v[142:143], v[130:131], 2, v[132:133]
	global_store_dword v[142:143], v144, off
.LBB3_13:
	s_or_b64 exec, exec, s[2:3]
	s_waitcnt lgkmcnt(0)
	v_exp_f32_e32 v142, v110
	v_exp_f32_e32 v144, v112
	v_exp_f32_e32 v145, v113
	v_exp_f32_e32 v143, v111
	v_exp_f32_e32 v156, v76
	v_exp_f32_e32 v157, v77
	v_pk_add_f32 v[144:145], v[144:145], 1.0 op_sel_hi:[1,0]
	v_pk_add_f32 v[148:149], v[142:143], 1.0 op_sel_hi:[1,0]
	v_rcp_f32_e64 v143, -v145
	v_rcp_f32_e64 v142, -v144
	v_rcp_f32_e64 v151, -v149
	v_rcp_f32_e64 v150, -v148
	v_pk_add_f32 v[156:157], v[156:157], 1.0 op_sel_hi:[1,0]
	v_pk_fma_f32 v[154:155], v[142:143], 2.0, 1.0 op_sel_hi:[1,0,0]
	v_rcp_f32_e64 v159, -v157
	v_pk_fma_f32 v[142:143], v[150:151], 2.0, 1.0 op_sel_hi:[1,0,0]
	v_exp_f32_e32 v150, v74
	v_exp_f32_e32 v151, v75
	v_rcp_f32_e64 v158, -v156
	v_cvt_pk_bf16_f32 v142, v142, v143
	v_cvt_pk_bf16_f32 v143, v154, v155
	v_pk_add_f32 v[150:151], v[150:151], 1.0 op_sel_hi:[1,0]
	v_pk_fma_f32 v[154:155], v[158:159], 2.0, 1.0 op_sel_hi:[1,0,0]
	v_rcp_f32_e64 v161, -v151
	v_rcp_f32_e64 v160, -v150
	v_pk_mul_f32 v[156:157], v[144:145], v[156:157]
	v_cvt_pk_bf16_f32 v145, v154, v155
	v_exp_f32_e32 v154, v102
	v_pk_fma_f32 v[158:159], v[160:161], 2.0, 1.0 op_sel_hi:[1,0,0]
	v_exp_f32_e32 v155, v103
	v_cvt_pk_bf16_f32 v144, v158, v159
	v_exp_f32_e32 v158, v104
	v_exp_f32_e32 v159, v105
	v_pk_mul_f32 v[148:149], v[148:149], v[150:151]
	v_pk_add_f32 v[154:155], v[154:155], 1.0 op_sel_hi:[1,0]
	v_pk_add_f32 v[112:113], v[112:113], 0 op_sel_hi:[1,0]
	v_pk_add_f32 v[158:159], v[158:159], 1.0 op_sel_hi:[1,0]
	v_rcp_f32_e64 v165, -v155
	v_rcp_f32_e64 v163, -v159
	v_rcp_f32_e64 v162, -v158
	v_rcp_f32_e64 v164, -v154
	v_pk_mul_f32 v[148:149], v[148:149], v[154:155]
	v_pk_mul_f32 v[154:155], v[156:157], v[158:159]
	v_exp_f32_e32 v156, v66
	v_exp_f32_e32 v158, v68
	v_exp_f32_e32 v159, v69
	v_exp_f32_e32 v157, v67
	v_pk_add_f32 v[110:111], v[110:111], 0 op_sel_hi:[1,0]
	v_pk_add_f32 v[150:151], v[112:113], v[76:77]
	v_pk_add_f32 v[160:161], v[110:111], v[74:75]
	v_pk_add_f32 v[104:105], v[150:151], v[104:105]
	v_pk_add_f32 v[150:151], v[158:159], 1.0 op_sel_hi:[1,0]
	v_pk_add_f32 v[156:157], v[156:157], 1.0 op_sel_hi:[1,0]
	v_pk_add_f32 v[102:103], v[160:161], v[102:103]
	v_rcp_f32_e64 v159, -v151
	v_rcp_f32_e64 v158, -v150
	v_rcp_f32_e64 v161, -v157
	v_rcp_f32_e64 v160, -v156
	v_permlane16_swap_b32_e32 v142, v144
	v_permlane16_swap_b32_e32 v143, v145
	ds_read_b128 v[110:113], v138
	ds_read_b128 v[74:77], v138 offset:64
	global_store_dwordx4 v228, v[142:145], s[58:59] offset:2048 nt
	v_pk_fma_f32 v[158:159], v[158:159], 2.0, 1.0 op_sel_hi:[1,0,0]
	v_pk_mul_f32 v[148:149], v[148:149], v[156:157]
	v_pk_fma_f32 v[144:145], v[162:163], 2.0, 1.0 op_sel_hi:[1,0,0]
	v_pk_fma_f32 v[142:143], v[164:165], 2.0, 1.0 op_sel_hi:[1,0,0]
	v_pk_mul_f32 v[150:151], v[154:155], v[150:151]
	v_cvt_pk_bf16_f32 v142, v142, v143
	v_cvt_pk_bf16_f32 v143, v144, v145
	v_pk_fma_f32 v[144:145], v[160:161], 2.0, 1.0 op_sel_hi:[1,0,0]
	v_exp_f32_e32 v160, v88
	v_cvt_pk_bf16_f32 v144, v144, v145
	v_cvt_pk_bf16_f32 v145, v158, v159
	v_exp_f32_e32 v158, v86
	v_exp_f32_e32 v159, v87
	v_permlane16_swap_b32_e32 v142, v144
	v_exp_f32_e32 v161, v89
	v_permlane16_swap_b32_e32 v143, v145
	v_pk_add_f32 v[158:159], v[158:159], 1.0 op_sel_hi:[1,0]
	v_pk_add_f32 v[154:155], v[104:105], v[68:69]
	v_pk_add_f32 v[156:157], v[102:103], v[66:67]
	ds_read_b128 v[102:105], v138 offset:128
	ds_read_b128 v[66:69], v138 offset:192
	v_rcp_f32_e64 v165, -v159
	v_rcp_f32_e64 v164, -v158
	global_store_dwordx4 v228, v[142:145], s[58:59] offset:2176 nt
	v_pk_mul_f32 v[148:149], v[148:149], v[158:159]
	v_exp_f32_e32 v152, v38
	v_exp_f32_e32 v158, v40
	v_exp_f32_e32 v159, v41
	v_exp_f32_e32 v153, v39
	v_pk_add_f32 v[160:161], v[160:161], 1.0 op_sel_hi:[1,0]
	v_pk_add_f32 v[88:89], v[154:155], v[88:89]
	v_rcp_f32_e64 v163, -v161
	v_rcp_f32_e64 v162, -v160
	v_pk_add_f32 v[154:155], v[158:159], 1.0 op_sel_hi:[1,0]
	v_pk_add_f32 v[152:153], v[152:153], 1.0 op_sel_hi:[1,0]
	v_pk_add_f32 v[86:87], v[156:157], v[86:87]
	v_rcp_f32_e64 v157, -v155
	v_rcp_f32_e64 v156, -v154
	v_rcp_f32_e64 v159, -v153
	v_rcp_f32_e64 v158, -v152
	v_pk_fma_f32 v[144:145], v[162:163], 2.0, 1.0 op_sel_hi:[1,0,0]
	v_pk_fma_f32 v[142:143], v[164:165], 2.0, 1.0 op_sel_hi:[1,0,0]
	v_pk_fma_f32 v[156:157], v[156:157], 2.0, 1.0 op_sel_hi:[1,0,0]
	v_cvt_pk_bf16_f32 v142, v142, v143
	v_cvt_pk_bf16_f32 v143, v144, v145
	v_pk_fma_f32 v[144:145], v[158:159], 2.0, 1.0 op_sel_hi:[1,0,0]
	v_exp_f32_e32 v158, v124
	v_cvt_pk_bf16_f32 v144, v144, v145
	v_cvt_pk_bf16_f32 v145, v156, v157
	v_exp_f32_e32 v156, v122
	v_exp_f32_e32 v159, v125
	v_exp_f32_e32 v157, v123
	v_pk_mul_f32 v[150:151], v[150:151], v[160:161]
	v_pk_mul_f32 v[150:151], v[150:151], v[154:155]
	v_pk_mul_f32 v[148:149], v[148:149], v[152:153]
	v_pk_add_f32 v[158:159], v[158:159], 1.0 op_sel_hi:[1,0]
	v_pk_add_f32 v[156:157], v[156:157], 1.0 op_sel_hi:[1,0]
	v_rcp_f32_e64 v163, -v157
	v_rcp_f32_e64 v162, -v156
	v_pk_mul_f32 v[146:147], v[148:149], v[156:157]
	v_pk_mul_f32 v[148:149], v[150:151], v[158:159]
	v_exp_f32_e32 v150, v50
	v_exp_f32_e32 v156, v52
	v_exp_f32_e32 v157, v53
	v_exp_f32_e32 v151, v51
	v_pk_add_f32 v[152:153], v[88:89], v[40:41]
	v_pk_add_f32 v[154:155], v[86:87], v[38:39]
	v_pk_add_f32 v[124:125], v[152:153], v[124:125]
	v_pk_add_f32 v[152:153], v[156:157], 1.0 op_sel_hi:[1,0]
	v_pk_add_f32 v[150:151], v[150:151], 1.0 op_sel_hi:[1,0]
	v_pk_mul_f32 v[148:149], v[148:149], v[152:153]
	v_pk_mul_f32 v[146:147], v[146:147], v[150:151]
	v_pk_add_f32 v[122:123], v[154:155], v[122:123]
	v_log_f32_e32 v131, v146
	v_log_f32_e32 v146, v147
	v_log_f32_e32 v147, v148
	v_log_f32_e32 v148, v149
	v_pk_add_f32 v[52:53], v[124:125], v[52:53]
	v_pk_add_f32 v[50:51], v[122:123], v[50:51]
	v_add_f32_e32 v122, v131, v146
	v_add_f32_e32 v123, v147, v148
	v_add_f32_e32 v50, v50, v51
	v_add_f32_e32 v51, v52, v53
	v_add_f32_e32 v122, v122, v123
	v_add_f32_e32 v50, v50, v51
	v_add_f32_e32 v122, 0xc2000000, v122
	v_mul_f32_e32 v131, 0xbeb17218, v50
	v_fmac_f32_e32 v131, 0x3f317218, v122
	v_rcp_f32_e64 v161, -v159
	v_rcp_f32_e64 v160, -v158
	ds_bpermute_b32 v148, v140, v131
	v_rcp_f32_e64 v155, -v153
	v_rcp_f32_e64 v154, -v152
	v_permlane16_swap_b32_e32 v142, v144
	v_permlane16_swap_b32_e32 v143, v145
	ds_read_b128 v[86:89], v138 offset:512
	ds_read_b128 v[38:41], v138 offset:576
	global_store_dwordx4 v228, v[142:145], s[62:63] offset:2048 nt
	v_rcp_f32_e64 v157, -v151
	v_rcp_f32_e64 v156, -v150
	v_pk_fma_f32 v[142:143], v[160:161], 2.0, 1.0 op_sel_hi:[1,0,0]
	v_pk_fma_f32 v[144:145], v[162:163], 2.0, 1.0 op_sel_hi:[1,0,0]
	s_waitcnt lgkmcnt(0)
	v_add_f32_e32 v131, v131, v148
	v_cvt_pk_bf16_f32 v144, v144, v145
	v_cvt_pk_bf16_f32 v145, v142, v143
	v_pk_fma_f32 v[142:143], v[154:155], 2.0, 1.0 op_sel_hi:[1,0,0]
	ds_read_b128 v[122:125], v138 offset:640
	ds_read_b128 v[50:53], v138 offset:704
	v_cvt_pk_bf16_f32 v147, v142, v143
	ds_bpermute_b32 v142, v139, v131
	v_pk_fma_f32 v[154:155], v[156:157], 2.0, 1.0 op_sel_hi:[1,0,0]
	v_permlane16_swap_b32_e32 v145, v147
	v_cvt_pk_bf16_f32 v146, v154, v155
	s_nop 1
	v_permlane16_swap_b32_e32 v144, v146
	global_store_dwordx4 v228, v[144:147], s[62:63] offset:2176 nt
	s_and_saveexec_b64 s[2:3], s[0:1]
	s_cbranch_execz .LBB3_15
	s_waitcnt lgkmcnt(0)
	v_add_f32_e32 v144, v131, v142
	v_mov_b32_e32 v131, v195
	v_lshl_add_u64 v[142:143], v[130:131], 2, v[132:133]
	global_store_dword v[142:143], v144, off offset:64
.LBB3_15:
	s_or_b64 exec, exec, s[2:3]
	s_waitcnt lgkmcnt(0)
	v_exp_f32_e32 v142, v98
	v_exp_f32_e32 v144, v100
	v_exp_f32_e32 v145, v101
	v_exp_f32_e32 v143, v99
	v_exp_f32_e32 v156, v64
	v_exp_f32_e32 v157, v65
	v_pk_add_f32 v[144:145], v[144:145], 1.0 op_sel_hi:[1,0]
	v_pk_add_f32 v[148:149], v[142:143], 1.0 op_sel_hi:[1,0]
	v_rcp_f32_e64 v143, -v145
	v_rcp_f32_e64 v142, -v144
	v_rcp_f32_e64 v151, -v149
	v_rcp_f32_e64 v150, -v148
	v_pk_add_f32 v[156:157], v[156:157], 1.0 op_sel_hi:[1,0]
	v_pk_fma_f32 v[154:155], v[142:143], 2.0, 1.0 op_sel_hi:[1,0,0]
	v_rcp_f32_e64 v159, -v157
	v_pk_fma_f32 v[142:143], v[150:151], 2.0, 1.0 op_sel_hi:[1,0,0]
	v_exp_f32_e32 v150, v62
	v_exp_f32_e32 v151, v63
	v_rcp_f32_e64 v158, -v156
	v_cvt_pk_bf16_f32 v142, v142, v143
	v_cvt_pk_bf16_f32 v143, v154, v155
	v_pk_add_f32 v[150:151], v[150:151], 1.0 op_sel_hi:[1,0]
	v_pk_fma_f32 v[154:155], v[158:159], 2.0, 1.0 op_sel_hi:[1,0,0]
	v_rcp_f32_e64 v161, -v151
	v_rcp_f32_e64 v160, -v150
	v_pk_mul_f32 v[156:157], v[144:145], v[156:157]
	v_cvt_pk_bf16_f32 v145, v154, v155
	v_exp_f32_e32 v154, v94
	v_pk_fma_f32 v[158:159], v[160:161], 2.0, 1.0 op_sel_hi:[1,0,0]
	v_exp_f32_e32 v155, v95
	v_cvt_pk_bf16_f32 v144, v158, v159
	v_exp_f32_e32 v158, v96
	v_exp_f32_e32 v159, v97
	v_pk_mul_f32 v[148:149], v[148:149], v[150:151]
	v_pk_add_f32 v[154:155], v[154:155], 1.0 op_sel_hi:[1,0]
	v_pk_add_f32 v[100:101], v[100:101], 0 op_sel_hi:[1,0]
	v_pk_add_f32 v[158:159], v[158:159], 1.0 op_sel_hi:[1,0]
	v_rcp_f32_e64 v165, -v155
	v_rcp_f32_e64 v163, -v159
	v_rcp_f32_e64 v162, -v158
	v_rcp_f32_e64 v164, -v154
	v_pk_mul_f32 v[148:149], v[148:149], v[154:155]
	v_pk_mul_f32 v[154:155], v[156:157], v[158:159]
	v_exp_f32_e32 v156, v54
	v_exp_f32_e32 v158, v56
	v_exp_f32_e32 v159, v57
	v_exp_f32_e32 v157, v55
	v_pk_add_f32 v[98:99], v[98:99], 0 op_sel_hi:[1,0]
	v_pk_add_f32 v[150:151], v[100:101], v[64:65]
	v_pk_add_f32 v[160:161], v[98:99], v[62:63]
	v_pk_add_f32 v[96:97], v[150:151], v[96:97]
	v_pk_add_f32 v[150:151], v[158:159], 1.0 op_sel_hi:[1,0]
	v_pk_add_f32 v[156:157], v[156:157], 1.0 op_sel_hi:[1,0]
	v_pk_add_f32 v[94:95], v[160:161], v[94:95]
	v_rcp_f32_e64 v159, -v151
	v_rcp_f32_e64 v158, -v150
	v_rcp_f32_e64 v161, -v157
	v_rcp_f32_e64 v160, -v156
	v_permlane16_swap_b32_e32 v142, v144
	v_permlane16_swap_b32_e32 v143, v145
	ds_read_b128 v[98:101], v138
	ds_read_b128 v[62:65], v138 offset:64
	global_store_dwordx4 v228, v[142:145], s[60:61] nt
	v_pk_fma_f32 v[158:159], v[158:159], 2.0, 1.0 op_sel_hi:[1,0,0]
	v_pk_mul_f32 v[148:149], v[148:149], v[156:157]
	v_pk_fma_f32 v[144:145], v[162:163], 2.0, 1.0 op_sel_hi:[1,0,0]
	v_pk_fma_f32 v[142:143], v[164:165], 2.0, 1.0 op_sel_hi:[1,0,0]
	v_pk_mul_f32 v[150:151], v[154:155], v[150:151]
	v_cvt_pk_bf16_f32 v142, v142, v143
	v_cvt_pk_bf16_f32 v143, v144, v145
	v_pk_fma_f32 v[144:145], v[160:161], 2.0, 1.0 op_sel_hi:[1,0,0]
	v_exp_f32_e32 v160, v84
	v_cvt_pk_bf16_f32 v144, v144, v145
	v_cvt_pk_bf16_f32 v145, v158, v159
	v_exp_f32_e32 v158, v82
	v_exp_f32_e32 v159, v83
	v_permlane16_swap_b32_e32 v142, v144
	v_exp_f32_e32 v161, v85
	v_permlane16_swap_b32_e32 v143, v145
	v_pk_add_f32 v[158:159], v[158:159], 1.0 op_sel_hi:[1,0]
	v_pk_add_f32 v[154:155], v[96:97], v[56:57]
	v_pk_add_f32 v[156:157], v[94:95], v[54:55]
	ds_read_b128 v[94:97], v138 offset:128
	ds_read_b128 v[54:57], v138 offset:192
	v_rcp_f32_e64 v165, -v159
	v_rcp_f32_e64 v164, -v158
	global_store_dwordx4 v228, v[142:145], s[60:61] offset:128 nt
	v_pk_mul_f32 v[148:149], v[148:149], v[158:159]
	v_exp_f32_e32 v152, v34
	v_exp_f32_e32 v158, v36
	v_exp_f32_e32 v159, v37
	v_exp_f32_e32 v153, v35
	v_pk_add_f32 v[160:161], v[160:161], 1.0 op_sel_hi:[1,0]
	v_pk_add_f32 v[84:85], v[154:155], v[84:85]
	v_rcp_f32_e64 v163, -v161
	v_rcp_f32_e64 v162, -v160
	v_pk_add_f32 v[154:155], v[158:159], 1.0 op_sel_hi:[1,0]
	v_pk_add_f32 v[152:153], v[152:153], 1.0 op_sel_hi:[1,0]
	v_pk_add_f32 v[82:83], v[156:157], v[82:83]
	v_rcp_f32_e64 v157, -v155
	v_rcp_f32_e64 v156, -v154
	v_rcp_f32_e64 v159, -v153
	v_rcp_f32_e64 v158, -v152
	v_pk_fma_f32 v[144:145], v[162:163], 2.0, 1.0 op_sel_hi:[1,0,0]
	v_pk_fma_f32 v[142:143], v[164:165], 2.0, 1.0 op_sel_hi:[1,0,0]
	v_pk_fma_f32 v[156:157], v[156:157], 2.0, 1.0 op_sel_hi:[1,0,0]
	v_cvt_pk_bf16_f32 v142, v142, v143
	v_cvt_pk_bf16_f32 v143, v144, v145
	v_pk_fma_f32 v[144:145], v[158:159], 2.0, 1.0 op_sel_hi:[1,0,0]
	v_exp_f32_e32 v158, v120
	v_cvt_pk_bf16_f32 v144, v144, v145
	v_cvt_pk_bf16_f32 v145, v156, v157
	v_exp_f32_e32 v156, v118
	v_exp_f32_e32 v159, v121
	v_exp_f32_e32 v157, v119
	v_pk_mul_f32 v[150:151], v[150:151], v[160:161]
	v_pk_mul_f32 v[150:151], v[150:151], v[154:155]
	v_pk_mul_f32 v[148:149], v[148:149], v[152:153]
	v_pk_add_f32 v[158:159], v[158:159], 1.0 op_sel_hi:[1,0]
	v_pk_add_f32 v[156:157], v[156:157], 1.0 op_sel_hi:[1,0]
	v_rcp_f32_e64 v163, -v157
	v_rcp_f32_e64 v162, -v156
	v_pk_mul_f32 v[146:147], v[148:149], v[156:157]
	v_pk_mul_f32 v[148:149], v[150:151], v[158:159]
	v_exp_f32_e32 v150, v46
	v_exp_f32_e32 v156, v48
	v_exp_f32_e32 v157, v49
	v_exp_f32_e32 v151, v47
	v_pk_add_f32 v[152:153], v[84:85], v[36:37]
	v_pk_add_f32 v[154:155], v[82:83], v[34:35]
	v_pk_add_f32 v[120:121], v[152:153], v[120:121]
	v_pk_add_f32 v[152:153], v[156:157], 1.0 op_sel_hi:[1,0]
	v_pk_add_f32 v[150:151], v[150:151], 1.0 op_sel_hi:[1,0]
	v_pk_mul_f32 v[148:149], v[148:149], v[152:153]
	v_pk_mul_f32 v[146:147], v[146:147], v[150:151]
	v_pk_add_f32 v[118:119], v[154:155], v[118:119]
	v_log_f32_e32 v131, v146
	v_log_f32_e32 v146, v147
	v_log_f32_e32 v147, v148
	v_log_f32_e32 v148, v149
	v_pk_add_f32 v[48:49], v[120:121], v[48:49]
	v_pk_add_f32 v[46:47], v[118:119], v[46:47]
	v_add_f32_e32 v118, v131, v146
	v_add_f32_e32 v119, v147, v148
	v_add_f32_e32 v46, v46, v47
	v_add_f32_e32 v47, v48, v49
	v_add_f32_e32 v118, v118, v119
	v_add_f32_e32 v46, v46, v47
	v_add_f32_e32 v118, 0xc2000000, v118
	v_mul_f32_e32 v131, 0xbeb17218, v46
	v_fmac_f32_e32 v131, 0x3f317218, v118
	v_rcp_f32_e64 v161, -v159
	v_rcp_f32_e64 v160, -v158
	ds_bpermute_b32 v148, v140, v131
	v_rcp_f32_e64 v155, -v153
	v_rcp_f32_e64 v154, -v152
	v_permlane16_swap_b32_e32 v142, v144
	v_permlane16_swap_b32_e32 v143, v145
	ds_read_b128 v[82:85], v138 offset:512
	ds_read_b128 v[34:37], v138 offset:576
	global_store_dwordx4 v228, v[142:145], s[64:65] nt
	v_rcp_f32_e64 v157, -v151
	v_rcp_f32_e64 v156, -v150
	v_pk_fma_f32 v[142:143], v[160:161], 2.0, 1.0 op_sel_hi:[1,0,0]
	v_pk_fma_f32 v[144:145], v[162:163], 2.0, 1.0 op_sel_hi:[1,0,0]
	s_waitcnt lgkmcnt(0)
	v_add_f32_e32 v131, v131, v148
	v_cvt_pk_bf16_f32 v144, v144, v145
	v_cvt_pk_bf16_f32 v145, v142, v143
	v_pk_fma_f32 v[142:143], v[154:155], 2.0, 1.0 op_sel_hi:[1,0,0]
	ds_read_b128 v[118:121], v138 offset:640
	ds_read_b128 v[46:49], v138 offset:704
	v_cvt_pk_bf16_f32 v147, v142, v143
	ds_bpermute_b32 v142, v139, v131
	v_pk_fma_f32 v[154:155], v[156:157], 2.0, 1.0 op_sel_hi:[1,0,0]
	v_permlane16_swap_b32_e32 v145, v147
	v_cvt_pk_bf16_f32 v146, v154, v155
	s_nop 1
	v_permlane16_swap_b32_e32 v144, v146
	global_store_dwordx4 v228, v[144:147], s[64:65] offset:128 nt
	s_and_saveexec_b64 s[2:3], s[0:1]
	s_cbranch_execz .LBB3_17
	s_waitcnt lgkmcnt(0)
	v_add_f32_e32 v144, v131, v142
	v_mov_b32_e32 v131, v195
	v_lshl_add_u64 v[142:143], v[130:131], 2, v[132:133]
	global_store_dword v[142:143], v144, off offset:512

.Lg1_noY:
	s_waitcnt lgkmcnt(0)
	v_exp_f32_e32 v142, v18
	v_exp_f32_e32 v144, v20
	v_exp_f32_e32 v145, v21
	v_exp_f32_e32 v143, v19
	v_exp_f32_e32 v154, v4
	v_exp_f32_e32 v155, v5
	v_pk_add_f32 v[144:145], v[144:145], 1.0 op_sel_hi:[1,0]
	v_pk_add_f32 v[148:149], v[142:143], 1.0 op_sel_hi:[1,0]
	v_rcp_f32_e64 v143, -v145
	v_rcp_f32_e64 v142, -v144
	v_rcp_f32_e64 v151, -v149
	v_rcp_f32_e64 v150, -v148
	v_pk_add_f32 v[154:155], v[154:155], 1.0 op_sel_hi:[1,0]
	v_pk_fma_f32 v[152:153], v[142:143], 2.0, 1.0 op_sel_hi:[1,0,0]
	v_rcp_f32_e64 v157, -v155
	v_pk_fma_f32 v[142:143], v[150:151], 2.0, 1.0 op_sel_hi:[1,0,0]
	v_exp_f32_e32 v150, v2
	v_exp_f32_e32 v151, v3
	v_rcp_f32_e64 v156, -v154
	v_cvt_pk_bf16_f32 v142, v142, v143
	v_cvt_pk_bf16_f32 v143, v152, v153
	v_pk_add_f32 v[150:151], v[150:151], 1.0 op_sel_hi:[1,0]
	v_pk_fma_f32 v[152:153], v[156:157], 2.0, 1.0 op_sel_hi:[1,0,0]
	v_rcp_f32_e64 v159, -v151
	v_rcp_f32_e64 v158, -v150
	v_pk_mul_f32 v[154:155], v[144:145], v[154:155]
	v_cvt_pk_bf16_f32 v145, v152, v153
	v_exp_f32_e32 v152, v26
	v_pk_fma_f32 v[156:157], v[158:159], 2.0, 1.0 op_sel_hi:[1,0,0]
	v_exp_f32_e32 v153, v27
	v_cvt_pk_bf16_f32 v144, v156, v157
	v_exp_f32_e32 v156, v28
	v_exp_f32_e32 v157, v29
	v_pk_mul_f32 v[148:149], v[148:149], v[150:151]
	v_pk_add_f32 v[152:153], v[152:153], 1.0 op_sel_hi:[1,0]
	v_pk_add_f32 v[20:21], v[20:21], 0 op_sel_hi:[1,0]
	v_pk_add_f32 v[156:157], v[156:157], 1.0 op_sel_hi:[1,0]
	v_rcp_f32_e64 v163, -v153
	v_rcp_f32_e64 v161, -v157
	v_rcp_f32_e64 v160, -v156
	v_rcp_f32_e64 v162, -v152
	v_pk_mul_f32 v[148:149], v[148:149], v[152:153]
	v_pk_mul_f32 v[152:153], v[154:155], v[156:157]
	v_exp_f32_e32 v154, v10
	v_exp_f32_e32 v156, v12
	v_exp_f32_e32 v157, v13
	v_exp_f32_e32 v155, v11
	v_pk_add_f32 v[18:19], v[18:19], 0 op_sel_hi:[1,0]
	v_pk_add_f32 v[150:151], v[20:21], v[4:5]
	v_pk_add_f32 v[158:159], v[18:19], v[2:3]
	v_pk_add_f32 v[28:29], v[150:151], v[28:29]
	v_pk_add_f32 v[150:151], v[156:157], 1.0 op_sel_hi:[1,0]
	v_pk_add_f32 v[154:155], v[154:155], 1.0 op_sel_hi:[1,0]
	v_pk_add_f32 v[26:27], v[158:159], v[26:27]
	v_rcp_f32_e64 v157, -v151
	v_rcp_f32_e64 v156, -v150
	v_rcp_f32_e64 v159, -v155
	v_rcp_f32_e64 v158, -v154
	v_permlane16_swap_b32_e32 v142, v144
	v_permlane16_swap_b32_e32 v143, v145
	ds_read_b128 v[18:21], v138
	ds_read_b128 v[2:5], v138 offset:64
	global_store_dwordx4 v228, v[142:145], s[60:61] offset:2048 nt
	v_pk_fma_f32 v[156:157], v[156:157], 2.0, 1.0 op_sel_hi:[1,0,0]
	v_pk_mul_f32 v[150:151], v[152:153], v[150:151]
	v_pk_fma_f32 v[144:145], v[160:161], 2.0, 1.0 op_sel_hi:[1,0,0]
	v_pk_fma_f32 v[142:143], v[162:163], 2.0, 1.0 op_sel_hi:[1,0,0]
	v_pk_mul_f32 v[148:149], v[148:149], v[154:155]
	v_cvt_pk_bf16_f32 v142, v142, v143
	v_cvt_pk_bf16_f32 v143, v144, v145
	v_pk_fma_f32 v[144:145], v[158:159], 2.0, 1.0 op_sel_hi:[1,0,0]
	v_exp_f32_e32 v158, v24
	v_cvt_pk_bf16_f32 v144, v144, v145
	v_cvt_pk_bf16_f32 v145, v156, v157
	v_exp_f32_e32 v156, v22
	v_exp_f32_e32 v159, v25
	v_exp_f32_e32 v157, v23
	v_permlane16_swap_b32_e32 v142, v144
	v_permlane16_swap_b32_e32 v143, v145
	v_pk_add_f32 v[158:159], v[158:159], 1.0 op_sel_hi:[1,0]
	v_pk_add_f32 v[156:157], v[156:157], 1.0 op_sel_hi:[1,0]
	v_pk_add_f32 v[152:153], v[28:29], v[12:13]
	v_pk_add_f32 v[154:155], v[26:27], v[10:11]
	ds_read_b128 v[26:29], v138 offset:128
	ds_read_b128 v[10:13], v138 offset:192
	global_store_dwordx4 v228, v[142:145], s[60:61] offset:2176 nt
	v_rcp_f32_e64 v161, -v159
	v_rcp_f32_e64 v160, -v158
	v_pk_mul_f32 v[144:145], v[148:149], v[156:157]
	v_pk_mul_f32 v[146:147], v[150:151], v[158:159]
	v_exp_f32_e32 v148, v6
	v_exp_f32_e32 v150, v8
	v_exp_f32_e32 v151, v9
	v_exp_f32_e32 v149, v7
	v_rcp_f32_e64 v163, -v157
	v_rcp_f32_e64 v162, -v156
	v_pk_add_f32 v[150:151], v[150:151], 1.0 op_sel_hi:[1,0]
	v_pk_add_f32 v[148:149], v[148:149], 1.0 op_sel_hi:[1,0]
	v_pk_add_f32 v[24:25], v[152:153], v[24:25]
	v_pk_add_f32 v[22:23], v[154:155], v[22:23]
	v_rcp_f32_e64 v153, -v151
	v_rcp_f32_e64 v152, -v150
	v_rcp_f32_e64 v155, -v149
	v_rcp_f32_e64 v154, -v148
	v_pk_fma_f32 v[136:137], v[160:161], 2.0, 1.0 op_sel_hi:[1,0,0]
	v_pk_fma_f32 v[134:135], v[162:163], 2.0, 1.0 op_sel_hi:[1,0,0]
	v_pk_fma_f32 v[152:153], v[152:153], 2.0, 1.0 op_sel_hi:[1,0,0]
	v_cvt_pk_bf16_f32 v134, v134, v135
	v_cvt_pk_bf16_f32 v135, v136, v137
	v_pk_fma_f32 v[136:137], v[154:155], 2.0, 1.0 op_sel_hi:[1,0,0]
	v_pk_mul_f32 v[144:145], v[144:145], v[148:149]
	v_cvt_pk_bf16_f32 v136, v136, v137
	v_cvt_pk_bf16_f32 v137, v152, v153
	v_exp_f32_e32 v152, v30
	v_exp_f32_e32 v153, v31
	v_exp_f32_e32 v154, v32
	v_exp_f32_e32 v155, v33
	v_pk_add_f32 v[152:153], v[152:153], 1.0 op_sel_hi:[1,0]
	v_exp_f32_e32 v142, v14
	v_rcp_f32_e64 v159, -v153
	v_rcp_f32_e64 v158, -v152
	v_pk_mul_f32 v[144:145], v[144:145], v[152:153]
	v_exp_f32_e32 v152, v16
	v_exp_f32_e32 v153, v17
	v_exp_f32_e32 v143, v15
	v_pk_mul_f32 v[146:147], v[146:147], v[150:151]
	v_pk_add_f32 v[148:149], v[24:25], v[8:9]
	v_pk_add_f32 v[150:151], v[22:23], v[6:7]
	v_pk_add_f32 v[154:155], v[154:155], 1.0 op_sel_hi:[1,0]
	v_pk_add_f32 v[32:33], v[148:149], v[32:33]
	v_pk_mul_f32 v[146:147], v[146:147], v[154:155]
	v_pk_add_f32 v[30:31], v[150:151], v[30:31]
	v_pk_add_f32 v[148:149], v[152:153], 1.0 op_sel_hi:[1,0]
	v_pk_add_f32 v[150:151], v[142:143], 1.0 op_sel_hi:[1,0]
	v_pk_mul_f32 v[146:147], v[146:147], v[148:149]
	v_pk_mul_f32 v[144:145], v[144:145], v[150:151]
	v_pk_add_f32 v[16:17], v[32:33], v[16:17]
	v_log_f32_e32 v131, v144
	v_log_f32_e32 v141, v145
	v_log_f32_e32 v144, v146
	v_log_f32_e32 v145, v147
	v_pk_add_f32 v[14:15], v[30:31], v[14:15]
	v_add_f32_e32 v30, v131, v141
	v_add_f32_e32 v14, v14, v15
	v_add_f32_e32 v31, v144, v145
	v_add_f32_e32 v15, v16, v17
	v_add_f32_e32 v30, v30, v31
	v_add_f32_e32 v14, v14, v15
	v_add_f32_e32 v30, 0xc2000000, v30
	v_mul_f32_e32 v131, 0xbeb17218, v14
	v_fmac_f32_e32 v131, 0x3f317218, v30
	v_rcp_f32_e64 v157, -v155
	v_rcp_f32_e64 v156, -v154
	ds_bpermute_b32 v140, v140, v131
	v_rcp_f32_e64 v153, -v149
	v_rcp_f32_e64 v152, -v148
	v_permlane16_swap_b32_e32 v134, v136
	v_permlane16_swap_b32_e32 v135, v137
	ds_read_b128 v[22:25], v138 offset:512
	ds_read_b128 v[6:9], v138 offset:576
	global_store_dwordx4 v228, v[134:137], s[64:65] offset:2048 nt
	v_rcp_f32_e64 v155, -v151
	v_rcp_f32_e64 v154, -v150
	v_pk_fma_f32 v[134:135], v[156:157], 2.0, 1.0 op_sel_hi:[1,0,0]
	s_waitcnt lgkmcnt(0)
	v_add_f32_e32 v131, v131, v140
	v_cvt_pk_bf16_f32 v143, v134, v135
	v_pk_fma_f32 v[134:135], v[152:153], 2.0, 1.0 op_sel_hi:[1,0,0]
	ds_read_b128 v[30:33], v138 offset:640
	ds_read_b128 v[14:17], v138 offset:704
	v_cvt_pk_bf16_f32 v145, v134, v135
	ds_bpermute_b32 v134, v139, v131
	v_pk_fma_f32 v[136:137], v[158:159], 2.0, 1.0 op_sel_hi:[1,0,0]
	v_permlane16_swap_b32_e32 v143, v145
	v_cvt_pk_bf16_f32 v142, v136, v137
	v_pk_fma_f32 v[136:137], v[154:155], 2.0, 1.0 op_sel_hi:[1,0,0]
	s_nop 0
	v_cvt_pk_bf16_f32 v144, v136, v137
	s_nop 1
	v_permlane16_swap_b32_e32 v142, v144
	global_store_dwordx4 v228, v[142:145], s[64:65] offset:2176 nt
	s_and_saveexec_b64 s[2:3], s[0:1]
	s_cbranch_execz .LBB3_5
	s_waitcnt lgkmcnt(0)
	v_add_f32_e32 v134, v131, v134
	v_mov_b32_e32 v131, v195
	v_lshl_add_u64 v[130:131], v[130:131], 2, v[132:133]
	global_store_dword v[130:131], v134, off offset:576
	s_branch .LBB3_5

	.amdhsa_kernel _Z7gemm1_kPKDF16_S0_PDF16_PKfPfS0_S1_
		.amdhsa_group_segment_fixed_size 0
		.amdhsa_private_segment_fixed_size 0
		.amdhsa_kernarg_size 56
		.amdhsa_user_sgpr_count 2
		.amdhsa_user_sgpr_dispatch_ptr 0
		.amdhsa_user_sgpr_queue_ptr 0
		.amdhsa_user_sgpr_kernarg_segment_ptr 1
		.amdhsa_user_sgpr_dispatch_id 0
		.amdhsa_user_sgpr_kernarg_preload_length 0
		.amdhsa_user_sgpr_kernarg_preload_offset 0
		.amdhsa_user_sgpr_private_segment_size 0
		.amdhsa_uses_dynamic_stack 0
		.amdhsa_enable_private_segment 0
		.amdhsa_system_sgpr_workgroup_id_x 1
		.amdhsa_system_sgpr_workgroup_id_y 0
		.amdhsa_system_sgpr_workgroup_id_z 0
		.amdhsa_system_sgpr_workgroup_info 0
		.amdhsa_system_vgpr_workitem_id 0
		.amdhsa_next_free_vgpr 232
		.amdhsa_next_free_sgpr 66
		.amdhsa_accum_offset 232
		.amdhsa_reserve_vcc 1
		.amdhsa_float_round_mode_32 0
		.amdhsa_float_round_mode_16_64 0
		.amdhsa_float_denorm_mode_32 3
		.amdhsa_float_denorm_mode_16_64 3
		.amdhsa_dx10_clamp 1
		.amdhsa_ieee_mode 1
		.amdhsa_fp16_overflow 0
		.amdhsa_tg_split 0
		.amdhsa_exception_fp_ieee_invalid_op 0
		.amdhsa_exception_fp_denorm_src 0
		.amdhsa_exception_fp_ieee_div_zero 0
		.amdhsa_exception_fp_ieee_overflow 0
		.amdhsa_exception_fp_ieee_underflow 0
		.amdhsa_exception_fp_ieee_inexact 0
		.amdhsa_exception_int_div_zero 0
	.end_amdhsa_kernel

amdhsa.kernels:
  - .agpr_count:     0
    .args:
      - .actual_access:  read_only
        .address_space:  global
        .offset:         0
        .size:           8
        .value_kind:     global_buffer
      - .actual_access:  read_only
        .address_space:  global
        .offset:         8
        .size:           8
        .value_kind:     global_buffer
      - .actual_access:  read_only
        .address_space:  global
        .offset:         16
        .size:           8
        .value_kind:     global_buffer
      - .actual_access:  write_only
        .address_space:  global
        .offset:         24
        .size:           8
        .value_kind:     global_buffer
      - .actual_access:  write_only
        .address_space:  global
        .offset:         32
        .size:           8
        .value_kind:     global_buffer
      - .actual_access:  write_only
        .address_space:  global
        .offset:         40
        .size:           8
        .value_kind:     global_buffer
      - .actual_access:  write_only
        .address_space:  global
        .offset:         48
        .size:           8
        .value_kind:     global_buffer
      - .actual_access:  read_only
        .address_space:  global
        .offset:         56
        .size:           8
        .value_kind:     global_buffer
      - .actual_access:  read_only
        .address_space:  global
        .offset:         64
        .size:           8
        .value_kind:     global_buffer
      - .actual_access:  write_only
        .address_space:  global
        .offset:         72
        .size:           8
        .value_kind:     global_buffer
    .group_segment_fixed_size: 8448
    .kernarg_segment_align: 8
    .kernarg_segment_size: 80
    .language:       OpenCL C
    .language_version:
      - 2
      - 0
    .max_flat_workgroup_size: 256
    .name:           _Z6prep_kPKfS0_S0_PDF16_S1_S1_S1_S1_S0_Pf
    .private_segment_fixed_size: 0
    .sgpr_count:     20
    .sgpr_spill_count: 0
    .symbol:         _Z6prep_kPKfS0_S0_PDF16_S1_S1_S1_S1_S0_Pf.kd
    .uniform_work_group_size: 1
    .uses_dynamic_stack: false
    .vgpr_count:     34
    .vgpr_spill_count: 0
    .wavefront_size: 64
  - .agpr_count:     0
    .args:
      - .actual_access:  read_only
        .address_space:  global
        .offset:         0
        .size:           8
        .value_kind:     global_buffer
      - .actual_access:  write_only
        .address_space:  global
        .offset:         8
        .size:           8
        .value_kind:     global_buffer
      - .actual_access:  read_only
        .address_space:  global
        .offset:         16
        .size:           8
        .value_kind:     global_buffer
      - .actual_access:  write_only
        .address_space:  global
        .offset:         24
        .size:           8
        .value_kind:     global_buffer
      - .offset:         32
        .size:           4
        .value_kind:     hidden_block_count_x
      - .offset:         36
        .size:           4
        .value_kind:     hidden_block_count_y
      - .offset:         40
        .size:           4
        .value_kind:     hidden_block_count_z
      - .offset:         44
        .size:           2
        .value_kind:     hidden_group_size_x
      - .offset:         46
        .size:           2
        .value_kind:     hidden_group_size_y
      - .offset:         48
        .size:           2
        .value_kind:     hidden_group_size_z
      - .offset:         50
        .size:           2
        .value_kind:     hidden_remainder_x
      - .offset:         52
        .size:           2
        .value_kind:     hidden_remainder_y
      - .offset:         54
        .size:           2
        .value_kind:     hidden_remainder_z
      - .offset:         72
        .size:           8
        .value_kind:     hidden_global_offset_x
      - .offset:         80
        .size:           8
        .value_kind:     hidden_global_offset_y
      - .offset:         88
        .size:           8
        .value_kind:     hidden_global_offset_z
      - .offset:         96
        .size:           2
        .value_kind:     hidden_grid_dims
    .group_segment_fixed_size: 0
    .kernarg_segment_align: 8
    .kernarg_segment_size: 288
    .language:       OpenCL C
    .language_version:
      - 2
      - 0
    .max_flat_workgroup_size: 1024
    .name:           _Z6post_kPKfPfPKDF16_PDF16_
    .private_segment_fixed_size: 0
    .sgpr_count:     14
    .sgpr_spill_count: 0
    .symbol:         _Z6post_kPKfPfPKDF16_PDF16_.kd
    .uniform_work_group_size: 1
    .uses_dynamic_stack: false
    .vgpr_count:     49
    .vgpr_spill_count: 0
    .wavefront_size: 64
  - .agpr_count:     0
    .args:
      - .actual_access:  read_only
        .address_space:  global
        .offset:         0
        .size:           8
        .value_kind:     global_buffer
      - .actual_access:  read_only
        .address_space:  global
        .offset:         8
        .size:           8
        .value_kind:     global_buffer
      - .actual_access:  write_only
        .address_space:  global
        .offset:         16
        .size:           8
        .value_kind:     global_buffer
      - .offset:         24
        .size:           4
        .value_kind:     hidden_block_count_x
      - .offset:         28
        .size:           4
        .value_kind:     hidden_block_count_y
      - .offset:         32
        .size:           4
        .value_kind:     hidden_block_count_z
      - .offset:         36
        .size:           2
        .value_kind:     hidden_group_size_x
      - .offset:         38
        .size:           2
        .value_kind:     hidden_group_size_y
      - .offset:         40
        .size:           2
        .value_kind:     hidden_group_size_z
      - .offset:         42
        .size:           2
        .value_kind:     hidden_remainder_x
      - .offset:         44
        .size:           2
        .value_kind:     hidden_remainder_y
      - .offset:         46
        .size:           2
        .value_kind:     hidden_remainder_z
      - .offset:         64
        .size:           8
        .value_kind:     hidden_global_offset_x
      - .offset:         72
        .size:           8
        .value_kind:     hidden_global_offset_y
      - .offset:         80
        .size:           8
        .value_kind:     hidden_global_offset_z
      - .offset:         88
        .size:           2
        .value_kind:     hidden_grid_dims
    .group_segment_fixed_size: 0
    .kernarg_segment_align: 8
    .kernarg_segment_size: 280
    .language:       OpenCL C
    .language_version:
      - 2
      - 0
    .max_flat_workgroup_size: 1024
    .name:           _Z8reduce_kPKDF16_PKfPf
    .private_segment_fixed_size: 0
    .sgpr_count:     16
    .sgpr_spill_count: 0
    .symbol:         _Z8reduce_kPKDF16_PKfPf.kd
    .uniform_work_group_size: 1
    .uses_dynamic_stack: false
    .vgpr_count:     42
    .vgpr_spill_count: 0
    .wavefront_size: 64
  - .agpr_count:     0
    .args:
      - .actual_access:  read_only
        .address_space:  global
        .offset:         0
        .size:           8
        .value_kind:     global_buffer
      - .actual_access:  read_only
        .address_space:  global
        .offset:         8
        .size:           8
        .value_kind:     global_buffer
      - .actual_access:  write_only
        .address_space:  global
        .offset:         16
        .size:           8
        .value_kind:     global_buffer
      - .address_space:  global
        .offset:         24
        .size:           8
        .value_kind:     global_buffer
      - .actual_access:  write_only
        .address_space:  global
        .offset:         32
        .size:           8
        .value_kind:     global_buffer
      - .actual_access:  read_only
        .address_space:  global
        .offset:         40
        .size:           8
        .value_kind:     global_buffer
      - .actual_access:  write_only
        .address_space:  global
        .offset:         48
        .size:           8
        .value_kind:     global_buffer
    .group_segment_fixed_size: 0
    .kernarg_segment_align: 8
    .kernarg_segment_size: 56
    .language:       OpenCL C
    .language_version:
      - 2
      - 0
    .max_flat_workgroup_size: 512
    .name:           _Z7gemm1_kPKDF16_S0_PDF16_PKfPfS0_S1_
    .private_segment_fixed_size: 0
    .sgpr_count:     72
    .sgpr_spill_count: 0
    .symbol:         _Z7gemm1_kPKDF16_S0_PDF16_PKfPfS0_S1_.kd
    .uniform_work_group_size: 1
    .uses_dynamic_stack: false
    .vgpr_count:     232
    .vgpr_spill_count: 0
    .wavefront_size: 64
  - .agpr_count:     0
    .args:
      - .actual_access:  read_only
        .address_space:  global
        .offset:         0
        .size:           8
        .value_kind:     global_buffer
      - .actual_access:  read_only
        .address_space:  global
        .offset:         8
        .size:           8
        .value_kind:     global_buffer
      - .offset:         16
        .size:           4
        .value_kind:     by_value
      - .offset:         20
        .size:           4
        .value_kind:     by_value
      - .offset:         24
        .size:           4
        .value_kind:     by_value
      - .offset:         28
        .size:           4
        .value_kind:     by_value
      - .actual_access:  read_only
        .address_space:  global
        .offset:         32
        .size:           8
        .value_kind:     global_buffer
      - .actual_access:  write_only
        .address_space:  global
        .offset:         40
        .size:           8
        .value_kind:     global_buffer
      - .actual_access:  read_only
        .address_space:  global
        .offset:         48
        .size:           8
        .value_kind:     global_buffer
      - .actual_access:  read_only
        .address_space:  global
        .offset:         56
        .size:           8
        .value_kind:     global_buffer
    .group_segment_fixed_size: 0
    .kernarg_segment_align: 8
    .kernarg_segment_size: 64
    .language:       OpenCL C
    .language_version:
      - 2
      - 0
    .max_flat_workgroup_size: 512
    .name:           _Z6gemm_kILi2EEvPKDF16_S1_iiiiPfPDF16_PKfS2_
    .private_segment_fixed_size: 0
    .sgpr_count:     60
    .sgpr_spill_count: 0
    .symbol:         _Z6gemm_kILi2EEvPKDF16_S1_iiiiPfPDF16_PKfS2_.kd
    .uniform_work_group_size: 1
    .uses_dynamic_stack: false
    .vgpr_count:     224
    .vgpr_spill_count: 0
    .wavefront_size: 64
  - .agpr_count:     0
    .args:
      - .actual_access:  read_only
        .address_space:  global
        .offset:         0
        .size:           8
        .value_kind:     global_buffer
      - .actual_access:  read_only
        .address_space:  global
        .offset:         8
        .size:           8
        .value_kind:     global_buffer
      - .offset:         16
        .size:           4
        .value_kind:     by_value
      - .offset:         20
        .size:           4
        .value_kind:     by_value
      - .offset:         24
        .size:           4
        .value_kind:     by_value
      - .offset:         28
        .size:           4
        .value_kind:     by_value
      - .actual_access:  read_only
        .address_space:  global
        .offset:         32
        .size:           8
        .value_kind:     global_buffer
      - .actual_access:  write_only
        .address_space:  global
        .offset:         40
        .size:           8
        .value_kind:     global_buffer
      - .actual_access:  read_only
        .address_space:  global
        .offset:         48
        .size:           8
        .value_kind:     global_buffer
      - .actual_access:  read_only
        .address_space:  global
        .offset:         56
        .size:           8
        .value_kind:     global_buffer
    .group_segment_fixed_size: 0
    .kernarg_segment_align: 8
    .kernarg_segment_size: 64
    .language:       OpenCL C
    .language_version:
      - 2
      - 0
    .max_flat_workgroup_size: 512
    .name:           _Z6gemm_kILi3EEvPKDF16_S1_iiiiPfPDF16_PKfS2_
    .private_segment_fixed_size: 0
    .sgpr_count:     51
    .sgpr_spill_count: 0
    .symbol:         _Z6gemm_kILi3EEvPKDF16_S1_iiiiPfPDF16_PKfS2_.kd
    .uniform_work_group_size: 1
    .uses_dynamic_stack: false
    .vgpr_count:     220
    .vgpr_spill_count: 0
    .wavefront_size: 64
